# helper triangular-inverse rewrite, with the code after the scan phase kept at the baseline's byte offsets (unreachable s_nop padding)
# speedup vs baseline: 1.0080x; 1.0080x over previous
.LBB0_1186:
	s_waitcnt lgkmcnt(0)
	s_barrier
	v_readlane_b32 s5, v255, 11
	v_readlane_b32 s1, v255, 25
	s_add_i32 s0, s5, 3
	s_addk_i32 s4, 0x60
	s_addk_i32 s1, 0x1800
	v_writelane_b32 v255, s1, 25
	s_cmpk_gt_u32 s5, 0x44
	v_add_u32_e32 v190, 0xffffffa0, v190
	s_cbranch_scc1 .LBB0_1188
	v_mov_b32_e32 v2, v18
	v_mov_b32_e32 v3, v19
	v_mov_b32_e32 v4, v20
	v_mov_b32_e32 v5, v21
	v_mov_b32_e32 v6, v22
	v_mov_b32_e32 v7, v23
	v_mov_b32_e32 v8, v24
	v_mov_b32_e32 v9, v25
	v_mov_b32_e32 v10, v26
	v_mov_b32_e32 v11, v27
	v_mov_b32_e32 v12, v28
	v_mov_b32_e32 v13, v29
	v_mov_b32_e32 v14, v30
	v_mov_b32_e32 v15, v31
	v_mov_b32_e32 v16, v32
	v_mov_b32_e32 v17, v33
	s_branch .LBB0_1114
	s_nop 0
	s_nop 0
	s_nop 0
	s_nop 0
	s_nop 0
	s_nop 0
	s_nop 0
	s_nop 0
	s_nop 0
	s_nop 0
	s_nop 0
	s_nop 0
	s_nop 0
	s_nop 0
	s_nop 0
	s_nop 0
	s_nop 0
	s_nop 0
	s_nop 0
	s_nop 0
	s_nop 0
	s_nop 0
	s_nop 0
	s_nop 0
	s_nop 0
	s_nop 0
	s_nop 0
	s_nop 0
	s_nop 0
	s_nop 0
	s_nop 0
	s_nop 0
	s_nop 0
	s_nop 0
	s_nop 0
	s_nop 0
	s_nop 0
	s_nop 0
	s_nop 0
	s_nop 0
	s_nop 0
	s_nop 0
	s_nop 0
	s_nop 0
	s_nop 0
	s_nop 0
	s_nop 0
	s_nop 0
	s_nop 0
	s_nop 0
	s_nop 0
	s_nop 0
	s_nop 0
	s_nop 0
	s_nop 0
	s_nop 0
	s_nop 0
	s_nop 0
	s_nop 0
	s_nop 0
	s_nop 0
	s_nop 0
	s_nop 0
	s_nop 0
	s_nop 0
	s_nop 0
	s_nop 0
	s_nop 0
	s_nop 0
	s_nop 0
	s_nop 0
	s_nop 0
	s_nop 0
	s_nop 0
	s_nop 0
	s_nop 0
	s_nop 0
	s_nop 0
	s_nop 0
	s_nop 0
	s_nop 0
	s_nop 0
	s_nop 0
	s_nop 0
	s_nop 0
	s_nop 0
	s_nop 0
	s_nop 0
	s_nop 0
	s_nop 0
	s_nop 0
	s_nop 0
	s_nop 0
	s_nop 0
	s_nop 0
	s_nop 0
	s_nop 0
	s_nop 0
	s_nop 0
	s_nop 0
	s_nop 0
	s_nop 0
	s_nop 0
	s_nop 0
	s_nop 0
	s_nop 0
	s_nop 0
	s_nop 0
	s_nop 0
	s_nop 0
	s_nop 0
	s_nop 0
	s_nop 0
	s_nop 0
	s_nop 0
	s_nop 0
	s_nop 0
	s_nop 0
	s_nop 0
	s_nop 0
	s_nop 0
	s_nop 0
	s_nop 0
	s_nop 0
	s_nop 0
	s_nop 0
	s_nop 0
	s_nop 0
	s_nop 0
	s_nop 0
	s_nop 0
	s_nop 0
	s_nop 0
	s_nop 0
	s_nop 0
	s_nop 0
	s_nop 0
	s_nop 0
	s_nop 0
	s_nop 0
	s_nop 0
	s_nop 0
	s_nop 0
	s_nop 0
	s_nop 0
	s_nop 0
	s_nop 0
	s_nop 0
	s_nop 0
	s_nop 0
	s_nop 0
	s_nop 0
	s_nop 0
	s_nop 0
	s_nop 0
	s_nop 0
	s_nop 0
	s_nop 0
	s_nop 0
	s_nop 0
	s_nop 0
	s_nop 0
	s_nop 0
	s_nop 0
	s_nop 0
	s_nop 0
	s_nop 0
	s_nop 0
	s_nop 0
	s_nop 0
	s_nop 0
	s_nop 0
	s_nop 0
	s_nop 0
	s_nop 0
	s_nop 0
	s_nop 0
	s_nop 0
	s_nop 0
	s_nop 0
	s_nop 0
	s_nop 0
	s_nop 0
	s_nop 0
	s_nop 0
	s_nop 0
	s_nop 0
	s_nop 0
	s_nop 0
	s_nop 0
	s_nop 0
	s_nop 0
	s_nop 0
	s_nop 0
	s_nop 0
	s_nop 0
	s_nop 0
	s_nop 0
	s_nop 0
	s_nop 0
	s_nop 0
	s_nop 0
	s_nop 0
	s_nop 0
	s_nop 0
	s_nop 0
	s_nop 0
	s_nop 0
	s_nop 0
	s_nop 0
	s_nop 0
	s_nop 0
	s_nop 0
	s_nop 0
	s_nop 0
	s_nop 0
	s_nop 0
	s_nop 0
	s_nop 0
	s_nop 0
	s_nop 0
	s_nop 0
	s_nop 0
	s_nop 0
	s_nop 0
	s_nop 0
	s_nop 0
	s_nop 0
	s_nop 0
	s_nop 0
	s_nop 0
	s_nop 0
	s_nop 0
	s_nop 0
	s_nop 0
	s_nop 0
	s_nop 0
	s_nop 0
	s_nop 0
	s_nop 0
	s_nop 0
	s_nop 0
	s_nop 0
	s_nop 0
	s_nop 0
	s_nop 0
	s_nop 0
	s_nop 0
	s_nop 0
	s_nop 0
	s_nop 0
	s_nop 0
	s_nop 0
	s_nop 0
	s_nop 0
	s_nop 0
	s_nop 0
	s_nop 0
	s_nop 0
	s_nop 0
	s_nop 0
	s_nop 0
	s_nop 0
	s_nop 0
	s_nop 0
	s_nop 0
	s_nop 0
	s_nop 0
	s_nop 0
	s_nop 0
	s_nop 0
	s_nop 0
	s_nop 0
	s_nop 0
	s_nop 0
	s_nop 0
	s_nop 0
	s_nop 0
	s_nop 0
	s_nop 0
	s_nop 0
	s_nop 0
	s_nop 0
	s_nop 0
	s_nop 0
	s_nop 0
	s_nop 0
	s_nop 0
	s_nop 0
	s_nop 0
	s_nop 0
	s_nop 0
	s_nop 0
	s_nop 0
	s_nop 0
	s_nop 0
	s_nop 0
	s_nop 0
	s_nop 0
	s_nop 0
	s_nop 0
	s_nop 0
	s_nop 0
	s_nop 0
	s_nop 0
	s_nop 0
	s_nop 0
	s_nop 0
	s_nop 0
	s_nop 0
	s_nop 0
	s_nop 0
	s_nop 0
	s_nop 0
	s_nop 0
	s_nop 0
	s_nop 0
	s_nop 0
	s_nop 0
	s_nop 0
	s_nop 0
	s_nop 0
	s_nop 0
	s_nop 0
	s_nop 0
	s_nop 0
	s_nop 0
	s_nop 0
	s_nop 0
	s_nop 0
	s_nop 0
	s_nop 0
	s_nop 0
	s_nop 0
	s_nop 0
	s_nop 0
	s_nop 0
	s_nop 0
	s_nop 0
	s_nop 0
	s_nop 0
	s_nop 0
	s_nop 0
	s_nop 0
	s_nop 0
	s_nop 0
	s_nop 0
	s_nop 0
	s_nop 0
	s_nop 0
	s_nop 0
	s_nop 0
	s_nop 0
	s_nop 0
	s_nop 0
	s_nop 0
	s_nop 0
	s_nop 0
	s_nop 0
	s_nop 0
	s_nop 0
	s_nop 0
	s_nop 0
	s_nop 0
	s_nop 0
	s_nop 0
	s_nop 0
	s_nop 0
	s_nop 0
	s_nop 0
	s_nop 0
	s_nop 0
	s_nop 0
	s_nop 0
	s_nop 0
	s_nop 0
	s_nop 0
	s_nop 0
	s_nop 0
	s_nop 0
	s_nop 0
	s_nop 0
	s_nop 0
	s_nop 0
	s_nop 0
	s_nop 0
	s_nop 0
	s_nop 0
	s_nop 0
	s_nop 0
	s_nop 0
	s_nop 0
	s_nop 0
	s_nop 0
	s_nop 0
	s_nop 0
	s_nop 0
	s_nop 0
	s_nop 0
	s_nop 0
	s_nop 0
	s_nop 0
	s_nop 0
	s_nop 0
	s_nop 0
	s_nop 0
	s_nop 0
	s_nop 0
	s_nop 0
	s_nop 0
	s_nop 0
	s_nop 0
	s_nop 0
	s_nop 0
	s_nop 0
	s_nop 0
	s_nop 0
	s_nop 0
	s_nop 0
	s_nop 0
	s_nop 0
	s_nop 0
	s_nop 0
	s_nop 0
	s_nop 0
	s_nop 0
	s_nop 0
	s_nop 0
	s_nop 0
	s_nop 0
	s_nop 0
	s_nop 0
	s_nop 0
	s_nop 0
	s_nop 0
	s_nop 0
	s_nop 0
	s_nop 0
	s_nop 0
	s_nop 0
	s_nop 0
	s_nop 0
	s_nop 0
	s_nop 0
	s_nop 0
	s_nop 0
	s_nop 0
	s_nop 0
	s_nop 0
	s_nop 0
	s_nop 0
	s_nop 0
	s_nop 0
	s_nop 0
	s_nop 0
	s_nop 0
	s_nop 0
	s_nop 0
	s_nop 0
	s_nop 0
	s_nop 0
	s_nop 0
	s_nop 0
	s_nop 0
	s_nop 0
	s_nop 0
	s_nop 0
	s_nop 0
	s_nop 0
	s_nop 0
	s_nop 0
	s_nop 0
	s_nop 0
	s_nop 0
	s_nop 0
	s_nop 0
	s_nop 0
	s_nop 0
	s_nop 0
	s_nop 0
	s_nop 0
	s_nop 0
	s_nop 0
	s_nop 0
	s_nop 0
	s_nop 0
	s_nop 0
	s_nop 0
	s_nop 0
	s_nop 0
	s_nop 0
	s_nop 0
	s_nop 0
	s_nop 0
	s_nop 0
	s_nop 0
	s_nop 0
	s_nop 0
	s_nop 0
	s_nop 0
	s_nop 0
	s_nop 0
	s_nop 0
	s_nop 0
	s_nop 0
	s_nop 0
	s_nop 0
	s_nop 0
	s_nop 0
	s_nop 0
	s_nop 0
	s_nop 0
	s_nop 0
	s_nop 0
	s_nop 0
	s_nop 0
	s_nop 0
	s_nop 0
	s_nop 0
	s_nop 0
	s_nop 0
	s_nop 0
	s_nop 0
	s_nop 0
	s_nop 0
	s_nop 0
	s_nop 0
	s_nop 0
	s_nop 0
	s_nop 0
	s_nop 0
	s_nop 0
	s_nop 0
	s_nop 0
	s_nop 0
	s_nop 0
	s_nop 0
	s_nop 0
	s_nop 0
	s_nop 0
	s_nop 0
	s_nop 0
	s_nop 0
	s_nop 0
	s_nop 0
	s_nop 0
	s_nop 0
	s_nop 0
	s_nop 0
	s_nop 0
	s_nop 0
	s_nop 0
	s_nop 0
	s_nop 0
	s_nop 0
	s_nop 0
	s_nop 0
	s_nop 0
	s_nop 0
	s_nop 0
	s_nop 0
	s_nop 0
	s_nop 0
	s_nop 0
	s_nop 0
	s_nop 0
	s_nop 0
	s_nop 0
	s_nop 0
	s_nop 0
	s_nop 0
	s_nop 0
	s_nop 0
	s_nop 0
	s_nop 0
	s_nop 0
	s_nop 0
	s_nop 0
	s_nop 0
	s_nop 0
	s_nop 0
	s_nop 0
	s_nop 0
	s_nop 0
	s_nop 0
	s_nop 0
	s_nop 0
	s_nop 0
	s_nop 0
	s_nop 0
	s_nop 0
	s_nop 0
	s_nop 0
	s_nop 0
	s_nop 0
	s_nop 0
	s_nop 0
	s_nop 0
	s_nop 0
	s_nop 0
	s_nop 0
	s_nop 0
	s_nop 0
	s_nop 0
	s_nop 0
	s_nop 0
	s_nop 0
	s_nop 0
	s_nop 0
	s_nop 0
	s_nop 0
	s_nop 0
	s_nop 0
	s_nop 0
	s_nop 0
	s_nop 0
	s_nop 0
	s_nop 0
	s_nop 0
	s_nop 0
	s_nop 0
	s_nop 0
	s_nop 0
	s_nop 0
	s_nop 0
	s_nop 0
	s_nop 0
	s_nop 0
	s_nop 0
	s_nop 0
	s_nop 0
	s_nop 0
	s_nop 0
	s_nop 0
	s_nop 0
	s_nop 0
	s_nop 0
	s_nop 0
	s_nop 0
	s_nop 0
	s_nop 0
	s_nop 0
	s_nop 0
	s_nop 0
	s_nop 0
	s_nop 0
	s_nop 0
	s_nop 0
	s_nop 0
	s_nop 0
	s_nop 0
	s_nop 0
	s_nop 0
	s_nop 0
	s_nop 0
	s_nop 0
	s_nop 0
	s_nop 0
	s_nop 0
	s_nop 0
	s_nop 0
	s_nop 0
	s_nop 0
	s_nop 0
	s_nop 0
	s_nop 0
	s_nop 0
	s_nop 0
	s_nop 0
	s_nop 0
	s_nop 0
	s_nop 0
	s_nop 0
	s_nop 0
	s_nop 0
	s_nop 0
	s_nop 0
	s_nop 0
	s_nop 0
	s_nop 0
	s_nop 0
	s_nop 0
	s_nop 0
	s_nop 0
	s_nop 0
	s_nop 0
	s_nop 0
	s_nop 0
	s_nop 0
	s_nop 0
	s_nop 0
	s_nop 0
	s_nop 0
	s_nop 0
	s_nop 0
	s_nop 0
	s_nop 0
	s_nop 0
	s_nop 0
	s_nop 0
	s_nop 0
	s_nop 0
	s_nop 0
	s_nop 0
	s_nop 0
	s_nop 0
	s_nop 0
	s_nop 0
	s_nop 0
	s_nop 0
	s_nop 0
	s_nop 0
	s_nop 0
	s_nop 0
	s_nop 0
	s_nop 0
	s_nop 0
	s_nop 0
	s_nop 0
	s_nop 0
	s_nop 0
	s_nop 0
	s_nop 0
	s_nop 0
	s_nop 0
	s_nop 0
	s_nop 0
	s_nop 0
	s_nop 0
	s_nop 0
	s_nop 0
	s_nop 0
	s_nop 0
	s_nop 0
	s_nop 0
	s_nop 0
	s_nop 0
	s_nop 0
	s_nop 0
	s_nop 0
	s_nop 0
	s_nop 0
	s_nop 0
	s_nop 0
	s_nop 0
	s_nop 0
	s_nop 0
	s_nop 0
	s_nop 0
	s_nop 0
	s_nop 0
	s_nop 0
	s_nop 0
	s_nop 0
	s_nop 0
	s_nop 0
	s_nop 0
	s_nop 0
	s_nop 0
	s_nop 0
	s_nop 0
	s_nop 0
	s_nop 0
	s_nop 0
	s_nop 0
	s_nop 0
	s_nop 0
	s_nop 0
	s_nop 0
	s_nop 0
	s_nop 0
	s_nop 0
	s_nop 0
	s_nop 0
	s_nop 0
	s_nop 0
	s_nop 0
	s_nop 0
	s_nop 0
	s_nop 0
	s_nop 0
	s_nop 0
	s_nop 0
	s_nop 0
	s_nop 0
	s_nop 0
	s_nop 0
	s_nop 0
	s_nop 0
	s_nop 0
	s_nop 0
	s_nop 0
	s_nop 0
	s_nop 0
	s_nop 0
	s_nop 0
	s_nop 0
	s_nop 0
	s_nop 0
	s_nop 0
	s_nop 0
	s_nop 0
	s_nop 0
	s_nop 0
	s_nop 0
	s_nop 0
	s_nop 0
	s_nop 0
	s_nop 0
	s_nop 0
	s_nop 0
	s_nop 0
	s_nop 0
	s_nop 0
	s_nop 0
	s_nop 0
	s_nop 0
	s_nop 0
	s_nop 0
	s_nop 0
	s_nop 0
	s_nop 0
	s_nop 0
	s_nop 0
	s_nop 0
	s_nop 0
	s_nop 0
	s_nop 0
	s_nop 0
	s_nop 0
	s_nop 0
	s_nop 0
	s_nop 0
	s_nop 0
	s_nop 0
	s_nop 0
	s_nop 0
	s_nop 0
	s_nop 0
	s_nop 0
	s_nop 0
	s_nop 0
	s_nop 0
	s_nop 0
	s_nop 0
	s_nop 0
	s_nop 0
	s_nop 0
	s_nop 0
	s_nop 0
	s_nop 0
	s_nop 0
	s_nop 0
	s_nop 0
	s_nop 0
	s_nop 0
	s_nop 0
	s_nop 0
	s_nop 0
	s_nop 0
	s_nop 0
	s_nop 0
	s_nop 0
	s_nop 0
	s_nop 0
	s_nop 0
	s_nop 0
	s_nop 0
	s_nop 0
	s_nop 0
	s_nop 0
	s_nop 0
	s_nop 0
	s_nop 0
	s_nop 0
	s_nop 0
	s_nop 0
	s_nop 0
	s_nop 0
	s_nop 0
	s_nop 0
	s_nop 0
	s_nop 0
	s_nop 0
	s_nop 0
	s_nop 0
	s_nop 0
	s_nop 0
	s_nop 0
	s_nop 0
	s_nop 0
	s_nop 0
	s_nop 0
	s_nop 0
	s_nop 0
	s_nop 0
	s_nop 0
	s_nop 0
	s_nop 0
	s_nop 0
	s_nop 0
	s_nop 0
	s_nop 0
	s_nop 0
	s_nop 0
	s_nop 0
	s_nop 0
	s_nop 0
	s_nop 0
	s_nop 0
	s_nop 0
	s_nop 0
	s_nop 0
	s_nop 0
	s_nop 0
	s_nop 0
	s_nop 0
	s_nop 0
	s_nop 0
	s_nop 0
	s_nop 0
	s_nop 0
	s_nop 0
	s_nop 0
	s_nop 0
	s_nop 0
	s_nop 0
	s_nop 0
	s_nop 0
	s_nop 0
	s_nop 0
	s_nop 0
	s_nop 0
	s_nop 0
	s_nop 0
	s_nop 0
	s_nop 0
	s_nop 0
	s_nop 0
	s_nop 0
	s_nop 0
	s_nop 0
	s_nop 0
	s_nop 0
	s_nop 0
	s_nop 0
	s_nop 0
	s_nop 0
	s_nop 0
	s_nop 0
	s_nop 0
	s_nop 0
	s_nop 0
	s_nop 0
	s_nop 0
	s_nop 0
	s_nop 0
	s_nop 0
	s_nop 0
	s_nop 0
	s_nop 0
	s_nop 0
	s_nop 0
	s_nop 0
	s_nop 0
	s_nop 0
	s_nop 0
	s_nop 0
	s_nop 0
	s_nop 0
	s_nop 0
	s_nop 0
	s_nop 0
	s_nop 0
	s_nop 0
	s_nop 0
	s_nop 0
	s_nop 0
	s_nop 0
	s_nop 0
	s_nop 0
	s_nop 0
	s_nop 0
	s_nop 0
	s_nop 0
	s_nop 0
	s_nop 0
	s_nop 0
	s_nop 0
	s_nop 0
	s_nop 0
	s_nop 0
	s_nop 0
	s_nop 0
	s_nop 0
	s_nop 0
	s_nop 0
	s_nop 0
	s_nop 0
	s_nop 0
	s_nop 0
	s_nop 0
	s_nop 0
	s_nop 0
	s_nop 0
	s_nop 0
	s_nop 0
	s_nop 0
	s_nop 0
	s_nop 0
	s_nop 0
	s_nop 0
	s_nop 0
	s_nop 0
	s_nop 0
	s_nop 0
	s_nop 0
	s_nop 0
	s_nop 0
	s_nop 0
	s_nop 0
	s_nop 0
	s_nop 0
	s_nop 0
	s_nop 0
	s_nop 0
	s_nop 0
	s_nop 0
	s_nop 0
	s_nop 0
	s_nop 0
	s_nop 0
	s_nop 0
	s_nop 0
	s_nop 0
	s_nop 0
	s_nop 0
	s_nop 0
	s_nop 0
	s_nop 0
	s_nop 0
	s_nop 0
	s_nop 0
	s_nop 0
	s_nop 0
	s_nop 0
	s_nop 0
	s_nop 0
	s_nop 0
	s_nop 0
	s_nop 0
	s_nop 0
	s_nop 0
	s_nop 0
	s_nop 0
	s_nop 0
	s_nop 0
	s_nop 0
	s_nop 0
	s_nop 0
	s_nop 0
	s_nop 0
	s_nop 0
	s_nop 0
	s_nop 0
	s_nop 0
	s_nop 0
	s_nop 0
	s_nop 0
	s_nop 0
	s_nop 0
	s_nop 0
	s_nop 0
	s_nop 0
	s_nop 0
	s_nop 0
	s_nop 0
	s_nop 0
	s_nop 0
	s_nop 0
	s_nop 0
	s_nop 0
	s_nop 0
	s_nop 0
	s_nop 0
	s_nop 0
	s_nop 0
	s_nop 0
	s_nop 0
	s_nop 0
	s_nop 0
	s_nop 0
	s_nop 0
	s_nop 0
	s_nop 0
	s_nop 0
	s_nop 0
	s_nop 0
	s_nop 0
	s_nop 0
	s_nop 0
	s_nop 0
	s_nop 0
	s_nop 0
	s_nop 0
	s_nop 0
	s_nop 0
	s_nop 0
	s_nop 0
	s_nop 0
	s_nop 0
	s_nop 0
	s_nop 0
	s_nop 0
	s_nop 0
	s_nop 0
	s_nop 0
	s_nop 0
	s_nop 0
	s_nop 0
	s_nop 0
	s_nop 0
	s_nop 0
	s_nop 0
	s_nop 0
	s_nop 0
	s_nop 0
	s_nop 0
	s_nop 0
	s_nop 0
	s_nop 0
	s_nop 0
	s_nop 0
	s_nop 0
	s_nop 0
	s_nop 0
	s_nop 0
	s_nop 0
	s_nop 0
	s_nop 0
	s_nop 0
	s_nop 0
	s_nop 0
	s_nop 0
	s_nop 0
	s_nop 0
	s_nop 0
	s_nop 0
	s_nop 0
	s_nop 0
	s_nop 0
	s_nop 0
	s_nop 0
	s_nop 0
	s_nop 0
	s_nop 0
	s_nop 0
	s_nop 0
	s_nop 0
	s_nop 0
	s_nop 0
	s_nop 0
	s_nop 0
	s_nop 0
	s_nop 0
	s_nop 0
	s_nop 0
	s_nop 0
	s_nop 0
	s_nop 0
	s_nop 0
	s_nop 0
	s_nop 0
	s_nop 0
	s_nop 0
	s_nop 0
	s_nop 0
	s_nop 0
	s_nop 0
	s_nop 0
	s_nop 0
	s_nop 0
	s_nop 0
	s_nop 0
	s_nop 0
	s_nop 0
	s_nop 0
	s_nop 0
	s_nop 0
	s_nop 0
	s_nop 0
	s_nop 0
	s_nop 0
	s_nop 0
	s_nop 0
	s_nop 0
	s_nop 0
	s_nop 0
	s_nop 0
	s_nop 0
	s_nop 0
	s_nop 0
	s_nop 0
	s_nop 0
	s_nop 0
	s_nop 0
	s_nop 0
	s_nop 0
	s_nop 0
	s_nop 0
	s_nop 0
	s_nop 0
	s_nop 0
	s_nop 0
	s_nop 0
	s_nop 0
	s_nop 0
	s_nop 0
	s_nop 0
	s_nop 0
	s_nop 0
	s_nop 0
	s_nop 0
	s_nop 0
	s_nop 0
	s_nop 0
	s_nop 0
	s_nop 0
	s_nop 0
	s_nop 0
	s_nop 0
	s_nop 0
	s_nop 0
	s_nop 0
	s_nop 0
	s_nop 0
	s_nop 0
	s_nop 0
	s_nop 0
	s_nop 0
	s_nop 0
	s_nop 0
	s_nop 0
	s_nop 0
	s_nop 0
	s_nop 0
	s_nop 0
	s_nop 0
	s_nop 0
	s_nop 0
	s_nop 0
	s_nop 0
	s_nop 0
	s_nop 0
	s_nop 0
	s_nop 0
	s_nop 0
	s_nop 0
	s_nop 0
	s_nop 0
	s_nop 0
	s_nop 0
	s_nop 0
	s_nop 0
	s_nop 0
	s_nop 0
	s_nop 0
	s_nop 0
	s_nop 0
	s_nop 0
	s_nop 0
	s_nop 0
	s_nop 0
	s_nop 0
	s_nop 0
	s_nop 0
	s_nop 0
	s_nop 0
	s_nop 0
	s_nop 0
	s_nop 0
	s_nop 0
	s_nop 0
	s_nop 0
	s_nop 0
	s_nop 0
	s_nop 0
	s_nop 0
	s_nop 0
	s_nop 0
	s_nop 0
	s_nop 0
	s_nop 0
	s_nop 0
	s_nop 0
	s_nop 0
	s_nop 0
	s_nop 0
	s_nop 0
	s_nop 0
	s_nop 0
	s_nop 0
	s_nop 0
	s_nop 0
	s_nop 0
	s_nop 0
	s_nop 0
	s_nop 0
	s_nop 0
	s_nop 0
	s_nop 0
	s_nop 0
	s_nop 0
	s_nop 0
	s_nop 0
	s_nop 0
	s_nop 0
	s_nop 0
	s_nop 0
	s_nop 0
	s_nop 0
	s_nop 0
	s_nop 0
	s_nop 0
	s_nop 0
	s_nop 0
	s_nop 0
	s_nop 0
	s_nop 0
	s_nop 0
	s_nop 0
	s_nop 0
	s_nop 0
	s_nop 0
	s_nop 0
	s_nop 0
	s_nop 0
	s_nop 0
	s_nop 0
	s_nop 0
	s_nop 0
	s_nop 0
	s_nop 0
	s_nop 0
	s_nop 0
	s_nop 0
	s_nop 0
	s_nop 0
	s_nop 0
	s_nop 0
	s_nop 0
	s_nop 0
	s_nop 0
	s_nop 0
	s_nop 0
	s_nop 0
	s_nop 0
	s_nop 0
	s_nop 0
	s_nop 0
	s_nop 0
	s_nop 0
	s_nop 0
	s_nop 0
	s_nop 0
	s_nop 0
	s_nop 0
	s_nop 0
	s_nop 0
	s_nop 0
	s_nop 0
	s_nop 0
	s_nop 0
	s_nop 0
	s_nop 0
	s_nop 0
	s_nop 0
	s_nop 0
	s_nop 0
	s_nop 0
	s_nop 0
	s_nop 0
	s_nop 0
	s_nop 0
	s_nop 0
	s_nop 0
	s_nop 0
	s_nop 0
	s_nop 0
	s_nop 0
	s_nop 0
	s_nop 0
	s_nop 0
	s_nop 0
	s_nop 0
	s_nop 0
	s_nop 0
	s_nop 0
	s_nop 0
	s_nop 0
	s_nop 0
	s_nop 0
	s_nop 0
	s_nop 0
	s_nop 0
	s_nop 0
	s_nop 0
	s_nop 0
	s_nop 0
	s_nop 0
	s_nop 0
	s_nop 0
	s_nop 0
	s_nop 0
	s_nop 0
	s_nop 0
	s_nop 0
	s_nop 0
	s_nop 0
	s_nop 0
	s_nop 0
	s_nop 0
	s_nop 0
	s_nop 0
	s_nop 0
	s_nop 0
	s_nop 0
	s_nop 0
	s_nop 0
	s_nop 0
	s_nop 0
	s_nop 0
	s_nop 0
	s_nop 0
	s_nop 0
	s_nop 0
	s_nop 0
	s_nop 0
	s_nop 0
	s_nop 0
	s_nop 0
	s_nop 0
	s_nop 0
	s_nop 0
	s_nop 0
	s_nop 0
	s_nop 0
	s_nop 0
	s_nop 0
	s_nop 0
	s_nop 0
	s_nop 0
	s_nop 0
	s_nop 0
	s_nop 0
	s_nop 0
	s_nop 0
	s_nop 0
	s_nop 0
	s_nop 0
	s_nop 0
	s_nop 0
	s_nop 0
	s_nop 0
	s_nop 0
	s_nop 0
	s_nop 0
	s_nop 0
	s_nop 0
	s_nop 0
	s_nop 0
	s_nop 0
	s_nop 0
	s_nop 0
	s_nop 0
	s_nop 0
	s_nop 0
	s_nop 0
	s_nop 0
	s_nop 0
	s_nop 0
	s_nop 0
	s_nop 0
	s_nop 0
	s_nop 0
	s_nop 0
	s_nop 0
	s_nop 0
	s_nop 0
	s_nop 0
	s_nop 0
	s_nop 0
	s_nop 0
	s_nop 0
	s_nop 0
	s_nop 0
	s_nop 0
	s_nop 0
	s_nop 0
	s_nop 0
	s_nop 0
	s_nop 0
	s_nop 0
	s_nop 0
	s_nop 0
	s_nop 0
	s_nop 0
	s_nop 0
	s_nop 0
	s_nop 0
	s_nop 0
	s_nop 0
	s_nop 0
	s_nop 0
	s_nop 0
	s_nop 0
	s_nop 0
	s_nop 0
	s_nop 0
	s_nop 0
	s_nop 0
	s_nop 0
	s_nop 0
	s_nop 0
	s_nop 0
	s_nop 0
	s_nop 0
	s_nop 0
	s_nop 0
	s_nop 0
	s_nop 0
	s_nop 0
	s_nop 0
	s_nop 0
	s_nop 0
	s_nop 0
	s_nop 0
	s_nop 0
	s_nop 0
	s_nop 0
	s_nop 0
	s_nop 0
	s_nop 0
	s_nop 0
	s_nop 0
	s_nop 0
	s_nop 0
	s_nop 0
	s_nop 0
	s_nop 0
	s_nop 0
	s_nop 0
	s_nop 0
	s_nop 0
	s_nop 0
	s_nop 0
	s_nop 0
	s_nop 0
	s_nop 0
	s_nop 0
	s_nop 0
	s_nop 0
	s_nop 0
	s_nop 0
	s_nop 0
	s_nop 0
	s_nop 0
	s_nop 0
	s_nop 0
	s_nop 0
	s_nop 0
	s_nop 0
	s_nop 0
	s_nop 0
	s_nop 0
	s_nop 0
	s_nop 0
	s_nop 0
	s_nop 0
	s_nop 0
	s_nop 0
	s_nop 0
	s_nop 0
	s_nop 0
	s_nop 0
	s_nop 0
	s_nop 0
	s_nop 0
	s_nop 0
